# P7 workgroup stagger: half of the workgroups (by bit 6 of the workgroup id) start the out-projection phase ~12 us later so their HBM-bound epilogues interleave with the other half's K loops
# baseline (speedup 1.0000x reference)
;     __device__ __forceinline__ void init(const void* A_, int slabA_, const void* Bt_, size_t estride_bytes, int rowbytes, const LAS int* ts_, int nN_, int G_, int c_) { slabA = slabA_; A = (const char*)A_; Bt = (const char*)Bt_; estride = estride_bytes; rowb = rowbytes; ts = ts_; nN = nN_; nwg = __builtin_amdgcn_readfirstlane(ts_[NE]) * nN_; G = G_; c = c_; }
; __device__ __forceinline__ int xcd_chunk(int L, int nwg) { const int q = nwg / NXCD, r = nwg % NXCD, xcd = L % NXCD, off = L / NXCD; return (xcd < r ? xcd * (q + 1) : r * (q + 1) + (xcd - r) * q) + off; }
;     __device__ __forceinline__ bool next(int i, Unit& u) const {
;         const int L = i * G + c; if (L >= nwg) return false;
;         const int wgid = xcd_chunk(L, nwg);
; __global__ void __launch_bounds__(512, 2) fwd_kernel(Params p) {
;     ...
;     if (IN(7)) {
;         pg8::DenseOrder S; S.init(MERGED, DM, WoutT, DM, T, DM, G, bx);
;         pg8::EpiOut E{p.in[I_X], X1, H2, p.in[I_GFFN]};
;         pg8::gemm_phase(lds, DM, DM, DM, S, E, wave);
.LBB0_901:
	s_or_b64 exec, exec, s[10:11]
	s_add_u32 s10, s28, 0x17800000
	s_addc_u32 s11, s29, 0
	s_add_u32 s14, s28, 0x9c000000
	s_addc_u32 s15, s29, 0
	s_andn2_b64 vcc, exec, s[6:7]
	s_waitcnt lgkmcnt(0)
	s_barrier
	v_mbcnt_lo_u32_b32 v0, -1, 0
	v_mbcnt_hi_u32_b32 v0, -1, v0
	s_cbranch_vccnz .LBB0_925
	s_bitcmp1_b32 s2, 6
	s_cbranch_scc0 .Lp7_nostag
	s_sleep 127
	s_sleep 127
	s_sleep 127
.Lp7_nostag:
	s_ashr_i32 s0, s2, 31
	s_lshr_b32 s0, s0, 29
	s_add_i32 s3, s2, s0
	s_and_b32 s0, s3, -8
	s_sub_i32 s0, s2, s0
	s_cmp_gt_i32 s0, -1
	s_cbranch_scc0 .LBB0_904
	s_lshl_b32 s8, s0, 6
	s_cbranch_execz .LBB0_905
	s_branch .LBB0_906
